# v74 plus w_out EpiNorm epilogue: gain vectors and residual rows prefetched before the row-sum exchange (five serial memory round trips removed from the tile tail)
# speedup vs baseline: 1.0178x; 1.0178x over previous
.LBB0_1530:
	v_mul_f32_e32 v0, v143, v143
	v_mul_f32_e32 v82, v145, v145
	v_fmac_f32_e32 v0, v142, v142
	v_fmac_f32_e32 v82, v144, v144
	v_add_f32_e32 v0, v0, v82
	v_mul_f32_e32 v82, v139, v139
	v_fmac_f32_e32 v82, v138, v138
	v_add_f32_e32 v0, v82, v0
	v_mul_f32_e32 v82, v141, v141
	v_fmac_f32_e32 v82, v140, v140
	v_add_f32_e32 v0, v82, v0
	v_mul_f32_e32 v82, v135, v135
	v_mul_f32_e32 v83, v137, v137
	v_fmac_f32_e32 v82, v134, v134
	v_fmac_f32_e32 v83, v136, v136
	v_add_f32_e32 v82, v82, v83
	v_mul_f32_e32 v83, v131, v131
	v_fmac_f32_e32 v83, v130, v130
	v_add_f32_e32 v82, v83, v82
	v_mul_f32_e32 v83, v133, v133
	v_fmac_f32_e32 v83, v132, v132
	v_add_f32_e32 v82, v83, v82
	v_mul_f32_e32 v83, v127, v127
	v_mul_f32_e32 v84, v129, v129
	v_fmac_f32_e32 v83, v126, v126
	v_fmac_f32_e32 v84, v128, v128
	v_add_f32_e32 v83, v83, v84
	v_mul_f32_e32 v84, v123, v123
	v_fmac_f32_e32 v84, v122, v122
	v_add_f32_e32 v83, v84, v83
	v_mul_f32_e32 v84, v125, v125
	v_fmac_f32_e32 v84, v124, v124
	v_add_f32_e32 v83, v84, v83
	v_mul_f32_e32 v84, v119, v119
	v_mul_f32_e32 v85, v121, v121
	v_fmac_f32_e32 v84, v118, v118
	v_fmac_f32_e32 v85, v120, v120
	v_add_f32_e32 v84, v84, v85
	v_mul_f32_e32 v85, v115, v115
	s_lshl_b32 s10, s37, 8
	v_readlane_b32 s0, v254, 31
	v_fmac_f32_e32 v85, v114, v114
	s_add_i32 s10, s10, s0
	s_lshl_b32 s0, s26, 4
	v_add_f32_e32 v84, v85, v84
	v_mul_f32_e32 v85, v117, v117
	s_add_i32 s0, s0, 0
	v_fmac_f32_e32 v85, v116, v116
	v_lshl_add_u32 v163, v97, 2, s0
	s_lshl_b32 s0, s29, 12
	v_add_f32_e32 v84, v85, v84
	v_add_f32_e32 v0, v82, v0
	v_add3_u32 v82, v163, s0, v146
	v_add_f32_e32 v83, v84, v83
	s_barrier
	ds_write2st64_b32 v82, v0, v83 offset1:4
	v_mul_f32_e32 v0, v111, v111
	v_mul_f32_e32 v83, v113, v113
	v_fmac_f32_e32 v0, v110, v110
	v_fmac_f32_e32 v83, v112, v112
	v_add_f32_e32 v0, v0, v83
	v_mul_f32_e32 v83, v107, v107
	v_fmac_f32_e32 v83, v106, v106
	v_add_f32_e32 v0, v83, v0
	v_mul_f32_e32 v83, v109, v109
	v_fmac_f32_e32 v83, v108, v108
	v_add_f32_e32 v0, v83, v0
	v_mul_f32_e32 v83, v103, v103
	v_mul_f32_e32 v84, v105, v105
	v_fmac_f32_e32 v83, v102, v102
	v_fmac_f32_e32 v84, v104, v104
	v_add_f32_e32 v83, v83, v84
	v_mul_f32_e32 v84, v99, v99
	v_fmac_f32_e32 v84, v98, v98
	v_add_f32_e32 v83, v84, v83
	v_mul_f32_e32 v84, v101, v101
	v_fmac_f32_e32 v84, v100, v100
	v_add_f32_e32 v83, v84, v83
	v_add_f32_e32 v0, v83, v0
	v_mul_f32_e32 v83, v79, v79
	v_mul_f32_e32 v84, v81, v81
	v_fmac_f32_e32 v83, v78, v78
	v_fmac_f32_e32 v84, v80, v80
	v_add_f32_e32 v83, v83, v84
	v_mul_f32_e32 v84, v75, v75
	v_fmac_f32_e32 v84, v74, v74
	v_add_f32_e32 v83, v84, v83
	v_mul_f32_e32 v84, v77, v77
	v_fmac_f32_e32 v84, v76, v76
	v_add_f32_e32 v83, v84, v83
	v_mul_f32_e32 v84, v71, v71
	v_mul_f32_e32 v85, v73, v73
	v_fmac_f32_e32 v84, v70, v70
	v_fmac_f32_e32 v85, v72, v72
	v_add_f32_e32 v84, v84, v85
	v_mul_f32_e32 v85, v67, v67
	v_fmac_f32_e32 v85, v66, v66
	v_add_f32_e32 v84, v85, v84
	v_mul_f32_e32 v85, v69, v69
	v_fmac_f32_e32 v85, v68, v68
	v_add_f32_e32 v84, v85, v84
	v_add_f32_e32 v83, v84, v83
	ds_write2st64_b32 v82, v0, v83 offset0:8 offset1:12
	v_mul_f32_e32 v0, v63, v63
	v_mul_f32_e32 v83, v65, v65
	v_fmac_f32_e32 v0, v62, v62
	v_fmac_f32_e32 v83, v64, v64
	v_add_f32_e32 v0, v0, v83
	v_mul_f32_e32 v83, v59, v59
	v_fmac_f32_e32 v83, v58, v58
	v_add_f32_e32 v0, v83, v0
	v_mul_f32_e32 v83, v61, v61
	v_fmac_f32_e32 v83, v60, v60
	v_add_f32_e32 v0, v83, v0
	v_mul_f32_e32 v83, v55, v55
	v_mul_f32_e32 v84, v57, v57
	v_fmac_f32_e32 v83, v54, v54
	v_fmac_f32_e32 v84, v56, v56
	v_add_f32_e32 v83, v83, v84
	v_mul_f32_e32 v84, v51, v51
	v_fmac_f32_e32 v84, v50, v50
	v_add_f32_e32 v83, v84, v83
	v_mul_f32_e32 v84, v53, v53
	v_fmac_f32_e32 v84, v52, v52
	v_add_f32_e32 v83, v84, v83
	v_add_f32_e32 v0, v83, v0
	v_mul_f32_e32 v83, v47, v47
	v_mul_f32_e32 v84, v49, v49
	v_fmac_f32_e32 v83, v46, v46
	v_fmac_f32_e32 v84, v48, v48
	v_add_f32_e32 v83, v83, v84
	v_mul_f32_e32 v84, v43, v43
	v_fmac_f32_e32 v84, v42, v42
	v_add_f32_e32 v83, v84, v83
	v_mul_f32_e32 v84, v45, v45
	v_fmac_f32_e32 v84, v44, v44
	v_add_f32_e32 v83, v84, v83
	v_mul_f32_e32 v84, v39, v39
	v_mul_f32_e32 v85, v41, v41
	v_fmac_f32_e32 v84, v38, v38
	v_fmac_f32_e32 v85, v40, v40
	v_add_f32_e32 v84, v84, v85
	v_mul_f32_e32 v85, v35, v35
	v_fmac_f32_e32 v85, v34, v34
	v_add_f32_e32 v84, v85, v84
	v_mul_f32_e32 v85, v37, v37
	v_fmac_f32_e32 v85, v36, v36
	v_add_f32_e32 v84, v85, v84
	v_add_f32_e32 v83, v84, v83
	ds_write2st64_b32 v82, v0, v83 offset0:32 offset1:36
	v_mul_f32_e32 v0, v31, v31
	v_mul_f32_e32 v83, v33, v33
	v_fmac_f32_e32 v0, v30, v30
	v_fmac_f32_e32 v83, v32, v32
	v_add_f32_e32 v0, v0, v83
	v_mul_f32_e32 v83, v27, v27
	v_fmac_f32_e32 v83, v26, v26
	v_add_f32_e32 v0, v83, v0
	v_mul_f32_e32 v83, v29, v29
	v_fmac_f32_e32 v83, v28, v28
	v_add_f32_e32 v0, v83, v0
	v_mul_f32_e32 v83, v23, v23
	v_mul_f32_e32 v84, v25, v25
	v_fmac_f32_e32 v83, v22, v22
	v_fmac_f32_e32 v84, v24, v24
	v_add_f32_e32 v83, v83, v84
	v_mul_f32_e32 v84, v19, v19
	v_fmac_f32_e32 v84, v18, v18
	v_add_f32_e32 v83, v84, v83
	v_mul_f32_e32 v84, v21, v21
	v_fmac_f32_e32 v84, v20, v20
	v_add_f32_e32 v83, v84, v83
	v_add_f32_e32 v0, v83, v0
	v_mul_f32_e32 v83, v15, v15
	v_mul_f32_e32 v84, v17, v17
	v_fmac_f32_e32 v83, v14, v14
	v_fmac_f32_e32 v84, v16, v16
	v_add_f32_e32 v83, v83, v84
	v_mul_f32_e32 v84, v11, v11
	v_fmac_f32_e32 v84, v10, v10
	v_add_f32_e32 v83, v84, v83
	v_mul_f32_e32 v84, v13, v13
	v_fmac_f32_e32 v84, v12, v12
	v_add_f32_e32 v83, v84, v83
	v_mul_f32_e32 v84, v7, v7
	v_mul_f32_e32 v85, v9, v9
	v_fmac_f32_e32 v84, v6, v6
	v_fmac_f32_e32 v85, v8, v8
	v_add_f32_e32 v84, v84, v85
	v_mul_f32_e32 v85, v3, v3
	v_fmac_f32_e32 v85, v2, v2
	v_add_f32_e32 v84, v85, v84
	v_mul_f32_e32 v85, v5, v5
	v_fmac_f32_e32 v85, v4, v4
	v_add_f32_e32 v84, v85, v84
	v_add_f32_e32 v83, v84, v83
	s_lshl_b32 s2, s26, 5
	s_lshl_b32 s3, s4, 8
	s_or_b32 s2, s3, s2
	v_lshl_or_b32 v224, v97, 3, s2
	v_ashrrev_i32_e32 v225, 31, v224
	v_readlane_b32 s2, v254, 12
	v_readlane_b32 s3, v254, 13
	s_lshl_b64 s[2:3], s[2:3], 2
	s_add_u32 s2, s21, s2
	s_addc_u32 s3, s22, s3
	v_lshl_add_u64 v[226:227], v[224:225], 2, s[2:3]
	global_load_dwordx4 v[196:199], v[226:227], off
	global_load_dwordx4 v[200:203], v[226:227], off offset:16
	global_load_dwordx4 v[204:207], v[226:227], off offset:512
	global_load_dwordx4 v[208:211], v[226:227], off offset:528
	v_readlane_b32 s2, v252, 12
	v_readlane_b32 s3, v252, 13
	v_lshlrev_b64 v[184:185], 1, v[224:225]
	s_nop 0
	v_lshl_add_u64 v[184:185], s[2:3], 0, v[184:185]
	v_add_u32_e32 v224, s10, v162
	v_mov_b32_e32 v226, v224
	v_ashrrev_i32_e32 v227, 31, v226
	v_lshlrev_b64 v[226:227], 11, v[226:227]
	v_lshl_add_u64 v[226:227], v[184:185], 0, v[226:227]
	global_load_dwordx4 v[166:169], v[226:227], off
	global_load_dwordx4 v[170:173], v[226:227], off offset:256
	v_or_b32_e32 v226, 16, v224
	v_ashrrev_i32_e32 v227, 31, v226
	v_lshlrev_b64 v[226:227], 11, v[226:227]
	v_lshl_add_u64 v[226:227], v[184:185], 0, v[226:227]
	global_load_dwordx4 v[150:153], v[226:227], off
	global_load_dwordx4 v[180:183], v[226:227], off offset:256
	v_or_b32_e32 v226, 32, v224
	v_ashrrev_i32_e32 v227, 31, v226
	v_lshlrev_b64 v[226:227], 11, v[226:227]
	v_lshl_add_u64 v[226:227], v[184:185], 0, v[226:227]
	global_load_dwordx4 v[212:215], v[226:227], off
	global_load_dwordx4 v[216:219], v[226:227], off offset:256
	v_or_b32_e32 v226, 48, v224
	v_ashrrev_i32_e32 v227, 31, v226
	v_lshlrev_b64 v[226:227], 11, v[226:227]
	v_lshl_add_u64 v[226:227], v[184:185], 0, v[226:227]
	global_load_dwordx4 v[220:223], v[226:227], off
	s_nop 0
	global_load_dwordx4 v[224:227], v[226:227], off offset:256
	ds_write2st64_b32 v82, v0, v83 offset0:40 offset1:44
	s_waitcnt lgkmcnt(0)
	s_barrier
	v_add_u32_e32 v154, s10, v96
	v_readfirstlane_b32 s11, v96
	v_cmp_gt_i32_e64 s[0:1], s23, v96
	v_lshl_add_u32 v164, v96, 6, 0
	v_ashrrev_i32_e32 v155, 31, v154
	s_and_saveexec_b64 s[2:3], s[0:1]
	s_cbranch_execz .LBB0_1532
	ds_read_b128 v[82:85], v164
	ds_read_b128 v[86:89], v164 offset:32
	ds_read_b128 v[90:93], v164 offset:16
	ds_read_b128 v[146:149], v164 offset:48
	v_readlane_b32 s6, v252, 35
	s_waitcnt lgkmcnt(0)
	v_mov_b32_e32 v94, v82
	v_mov_b32_e32 v95, v86
	v_mov_b32_e32 v86, v83
	v_pk_add_f32 v[82:83], v[94:95], v[86:87]
	v_mov_b32_e32 v86, v84
	v_mov_b32_e32 v87, v88
	v_mov_b32_e32 v88, v85
	v_pk_add_f32 v[84:85], v[86:87], v[88:89]
	v_mov_b32_e32 v86, v92
	v_pk_add_f32 v[82:83], v[82:83], v[84:85]
	v_mov_b32_e32 v84, v90
	v_mov_b32_e32 v85, v146
	v_mov_b32_e32 v146, v91
	v_mov_b32_e32 v87, v148
	v_mov_b32_e32 v148, v93
	v_pk_add_f32 v[84:85], v[84:85], v[146:147]
	v_pk_add_f32 v[86:87], v[86:87], v[148:149]
	v_readlane_b32 s7, v252, 36
	v_pk_add_f32 v[84:85], v[84:85], v[86:87]
	s_ashr_i32 s5, s4, 31
	v_pk_add_f32 v[82:83], v[82:83], v[84:85]
	v_lshl_add_u64 v[84:85], v[154:155], 4, s[6:7]
	v_pk_add_f32 v[82:83], v[82:83], v[82:83] op_sel:[0,1] op_sel_hi:[1,0]
	v_lshl_add_u64 v[84:85], s[4:5], 2, v[84:85]
	global_store_dword v[84:85], v82, off sc1

.LBB0_1543:
	s_or_b64 exec, exec, s[2:3]
	s_lshl_b32 s2, s26, 5
	s_lshl_b32 s3, s4, 8
	s_or_b32 s2, s3, s2
	v_lshl_or_b32 v146, v97, 3, s2
	v_readlane_b32 s2, v254, 12
	v_readlane_b32 s3, v254, 13
	s_lshl_b64 s[2:3], s[2:3], 2
	s_add_u32 s2, s21, s2
	s_addc_u32 s3, s22, s3
	v_ashrrev_i32_e32 v147, 31, v146
	v_lshl_add_u64 v[82:83], v[146:147], 2, s[2:3]
	v_add_u32_e32 v160, s10, v162
	v_readlane_b32 s2, v252, 12
	v_lshlrev_b64 v[156:157], 1, v[146:147]
	v_readlane_b32 s3, v252, 13
	v_ashrrev_i32_e32 v161, 31, v160
	v_lshlrev_b64 v[174:175], 11, v[160:161]
	v_lshl_add_u64 v[158:159], s[2:3], 0, v[156:157]
	s_waitcnt lgkmcnt(0)
	s_barrier
	v_lshl_add_u64 v[146:147], v[158:159], 0, v[174:175]
	s_waitcnt vmcnt(0)
	v_mov_b32_e32 v94, v196
	v_mov_b32_e32 v95, v197
	v_mov_b32_e32 v96, v198
	v_mov_b32_e32 v97, v199
	v_mov_b32_e32 v90, v200
	v_mov_b32_e32 v91, v201
	v_mov_b32_e32 v92, v202
	v_mov_b32_e32 v93, v203
	v_mov_b32_e32 v86, v204
	v_mov_b32_e32 v87, v205
	v_mov_b32_e32 v88, v206
	v_mov_b32_e32 v89, v207
	v_mov_b32_e32 v82, v208
	v_mov_b32_e32 v83, v209
	v_mov_b32_e32 v84, v210
	v_mov_b32_e32 v85, v211
	s_nop 0
	v_or_b32_e32 v146, 16, v160
	v_ashrrev_i32_e32 v147, 31, v146
	v_lshlrev_b64 v[146:147], 11, v[146:147]
	v_lshl_add_u64 v[146:147], v[158:159], 0, v[146:147]
	v_mov_b32_e32 v146, v180
	v_mov_b32_e32 v147, v181
	v_mov_b32_e32 v148, v182
	v_mov_b32_e32 v149, v183
	v_lshl_add_u32 v161, v162, 2, 0
	ds_read_b32 v0, v161 offset:16384
	s_waitcnt lgkmcnt(0)
	v_pk_mul_f32 v[142:143], v[142:143], v[0:1] op_sel_hi:[1,0]
	v_pk_mul_f32 v[144:145], v[144:145], v[0:1] op_sel_hi:[1,0]
	v_pk_mul_f32 v[140:141], v[140:141], v[0:1] op_sel_hi:[1,0]
	v_pk_mul_f32 v[138:139], v[138:139], v[0:1] op_sel_hi:[1,0]
	v_pk_mul_f32 v[134:135], v[134:135], v[0:1] op_sel_hi:[1,0]
	v_pk_mul_f32 v[136:137], v[136:137], v[0:1] op_sel_hi:[1,0]
	v_pk_mul_f32 v[130:131], v[130:131], v[0:1] op_sel_hi:[1,0]
	v_pk_mul_f32 v[132:133], v[132:133], v[0:1] op_sel_hi:[1,0]
	s_waitcnt vmcnt(0)
	v_lshlrev_b32_e32 v176, 16, v166
	v_and_b32_e32 v177, 0xffff0000, v166
	v_lshlrev_b32_e32 v166, 16, v167
	v_and_b32_e32 v167, 0xffff0000, v167
	v_lshlrev_b32_e32 v178, 16, v168
	v_and_b32_e32 v179, 0xffff0000, v168
	v_lshlrev_b32_e32 v168, 16, v169
	v_and_b32_e32 v169, 0xffff0000, v169
	v_pk_fma_f32 v[142:143], v[94:95], v[142:143], v[176:177]
	v_pk_fma_f32 v[144:145], v[96:97], v[144:145], v[166:167]
	v_pk_fma_f32 v[166:167], v[92:93], v[140:141], v[168:169]
	v_cvt_pk_bf16_f32 v140, v142, v143
	v_mul_f32_e32 v143, v143, v143
	v_fmac_f32_e32 v143, v142, v142
	v_mul_f32_e32 v142, v145, v145
	v_pk_fma_f32 v[138:139], v[90:91], v[138:139], v[178:179]
	v_fmac_f32_e32 v142, v144, v144
	v_cvt_pk_bf16_f32 v141, v144, v145
	v_add_f32_e32 v144, v143, v142
	v_cvt_pk_bf16_f32 v142, v138, v139
	v_mul_f32_e32 v139, v139, v139
	v_fmac_f32_e32 v139, v138, v138
	v_mul_f32_e32 v138, v167, v167
	v_fmac_f32_e32 v138, v166, v166
	v_add_f32_e32 v138, v139, v138
	v_add_f32_e32 v168, v138, v144
	v_lshl_add_u64 v[138:139], s[2:3], 0, v[174:175]
	v_cvt_pk_bf16_f32 v143, v166, v167
	v_lshl_add_u64 v[138:139], v[138:139], 0, v[156:157]
	global_store_dwordx4 v[138:139], v[140:143], off
	v_lshlrev_b32_e32 v144, 16, v172
	v_and_b32_e32 v145, 0xffff0000, v172
	v_lshlrev_b32_e32 v140, 16, v170
	v_and_b32_e32 v141, 0xffff0000, v170
	v_lshlrev_b32_e32 v142, 16, v171
	v_and_b32_e32 v143, 0xffff0000, v171
	v_lshlrev_b32_e32 v166, 16, v173
	v_and_b32_e32 v167, 0xffff0000, v173
	v_pk_fma_f32 v[136:137], v[88:89], v[136:137], v[142:143]
	v_pk_fma_f32 v[134:135], v[86:87], v[134:135], v[140:141]
	v_pk_fma_f32 v[140:141], v[84:85], v[132:133], v[166:167]
	v_pk_fma_f32 v[142:143], v[82:83], v[130:131], v[144:145]
	v_mul_f32_e32 v0, v135, v135
	v_mul_f32_e32 v132, v137, v137
	v_cvt_pk_bf16_f32 v130, v134, v135
	v_fmac_f32_e32 v0, v134, v134
	v_fmac_f32_e32 v132, v136, v136
	v_mul_f32_e32 v134, v143, v143
	v_mul_f32_e32 v135, v141, v141
	v_add_f32_e32 v0, v0, v132
	v_fmac_f32_e32 v134, v142, v142
	v_fmac_f32_e32 v135, v140, v140
	v_cvt_pk_bf16_f32 v131, v136, v137
	v_add_f32_e32 v0, v0, v168
	v_cvt_pk_bf16_f32 v132, v142, v143
	v_cvt_pk_bf16_f32 v133, v140, v141
	v_add_f32_e32 v134, v134, v135
	v_add_f32_e32 v0, v134, v0
	global_store_dwordx4 v[138:139], v[130:133], off offset:256
	v_lshlrev_b32_e32 v134, 16, v151
	v_and_b32_e32 v135, 0xffff0000, v151
	v_add_u32_e32 v130, v163, v165
	ds_write_b32 v130, v0
	ds_read_b32 v0, v161 offset:16448
	v_lshlrev_b32_e32 v132, 16, v150
	v_and_b32_e32 v133, 0xffff0000, v150
	v_lshlrev_b32_e32 v136, 16, v152
	v_and_b32_e32 v137, 0xffff0000, v152
	s_waitcnt lgkmcnt(0)
	v_pk_mul_f32 v[128:129], v[128:129], v[0:1] op_sel_hi:[1,0]
	v_lshlrev_b32_e32 v138, 16, v153
	v_and_b32_e32 v139, 0xffff0000, v153
	v_pk_mul_f32 v[126:127], v[126:127], v[0:1] op_sel_hi:[1,0]
	v_pk_fma_f32 v[128:129], v[96:97], v[128:129], v[134:135]
	v_pk_mul_f32 v[122:123], v[122:123], v[0:1] op_sel_hi:[1,0]
	v_pk_mul_f32 v[124:125], v[124:125], v[0:1] op_sel_hi:[1,0]
	v_or_b32_e32 v140, 16, v162
	v_pk_fma_f32 v[126:127], v[94:95], v[126:127], v[132:133]
	v_pk_fma_f32 v[132:133], v[92:93], v[124:125], v[138:139]
	v_pk_fma_f32 v[134:135], v[90:91], v[122:123], v[136:137]
	v_mul_f32_e32 v125, v129, v129
	v_add_u32_e32 v130, s10, v140
	v_cvt_pk_bf16_f32 v122, v126, v127
	v_cvt_pk_bf16_f32 v123, v128, v129
	v_mul_f32_e32 v124, v127, v127
	v_fmac_f32_e32 v125, v128, v128
	v_mul_f32_e32 v127, v135, v135
	v_mul_f32_e32 v128, v133, v133
	v_ashrrev_i32_e32 v131, 31, v130
	v_fmac_f32_e32 v124, v126, v126
	v_fmac_f32_e32 v127, v134, v134
	v_fmac_f32_e32 v128, v132, v132
	v_lshlrev_b64 v[130:131], 11, v[130:131]
	v_add_f32_e32 v126, v124, v125
	v_add_f32_e32 v127, v127, v128
	v_cvt_pk_bf16_f32 v125, v132, v133
	v_add_f32_e32 v132, v127, v126
	v_lshl_add_u64 v[126:127], s[2:3], 0, v[130:131]
	v_cvt_pk_bf16_f32 v124, v134, v135
	v_lshl_add_u64 v[126:127], v[126:127], 0, v[156:157]
	global_store_dwordx4 v[126:127], v[122:125], off
	v_pk_mul_f32 v[118:119], v[118:119], v[0:1] op_sel_hi:[1,0]
	v_pk_mul_f32 v[120:121], v[120:121], v[0:1] op_sel_hi:[1,0]
	v_lshlrev_b32_e32 v122, 16, v146
	v_and_b32_e32 v123, 0xffff0000, v146
	v_lshlrev_b32_e32 v124, 16, v147
	v_and_b32_e32 v125, 0xffff0000, v147
	v_lshlrev_b32_e32 v128, 16, v148
	v_and_b32_e32 v129, 0xffff0000, v148
	v_lshlrev_b32_e32 v130, 16, v149
	v_and_b32_e32 v131, 0xffff0000, v149
	v_pk_fma_f32 v[120:121], v[88:89], v[120:121], v[124:125]
	v_pk_fma_f32 v[118:119], v[86:87], v[118:119], v[122:123]
	v_pk_mul_f32 v[114:115], v[114:115], v[0:1] op_sel_hi:[1,0]
	v_pk_mul_f32 v[116:117], v[116:117], v[0:1] op_sel_hi:[1,0]
	v_pk_fma_f32 v[124:125], v[82:83], v[114:115], v[128:129]
	v_pk_fma_f32 v[122:123], v[84:85], v[116:117], v[130:131]
	v_mul_f32_e32 v0, v119, v119
	v_mul_f32_e32 v116, v121, v121
	v_cvt_pk_bf16_f32 v114, v118, v119
	v_fmac_f32_e32 v0, v118, v118
	v_fmac_f32_e32 v116, v120, v120
	v_mul_f32_e32 v118, v125, v125
	v_mul_f32_e32 v119, v123, v123
	v_add_f32_e32 v0, v0, v116
	v_fmac_f32_e32 v118, v124, v124
	v_fmac_f32_e32 v119, v122, v122
	v_cvt_pk_bf16_f32 v115, v120, v121
	v_add_f32_e32 v0, v0, v132
	v_cvt_pk_bf16_f32 v116, v124, v125
	v_cvt_pk_bf16_f32 v117, v122, v123
	v_add_f32_e32 v118, v118, v119
	v_add_f32_e32 v0, v118, v0
	global_store_dwordx4 v[126:127], v[114:117], off offset:256
	s_nop 1
	v_lshl_add_u32 v114, v140, 6, v163
	ds_write_b32 v114, v0
	s_waitcnt vmcnt(4)
	v_mov_b32_e32 v122, v212
	v_mov_b32_e32 v123, v213
	v_mov_b32_e32 v124, v214
	v_mov_b32_e32 v125, v215
	v_mov_b32_e32 v126, v216
	v_mov_b32_e32 v127, v217
	v_mov_b32_e32 v128, v218
	v_mov_b32_e32 v129, v219
	v_mov_b32_e32 v118, v220
	v_mov_b32_e32 v119, v221
	v_mov_b32_e32 v120, v222
	v_mov_b32_e32 v121, v223
	v_mov_b32_e32 v114, v224
	v_mov_b32_e32 v115, v225
	v_mov_b32_e32 v116, v226
	v_mov_b32_e32 v117, v227
	v_add_u32_e32 v184, 0x80, v160
	v_ashrrev_i32_e32 v185, 31, v184
	v_lshlrev_b64 v[184:185], 11, v[184:185]
	v_lshl_add_u64 v[184:185], v[158:159], 0, v[184:185]
	global_load_dwordx4 v[212:215], v[184:185], off
	global_load_dwordx4 v[216:219], v[184:185], off offset:256
	v_add_u32_e32 v184, 0x90, v160
	v_ashrrev_i32_e32 v185, 31, v184
	v_lshlrev_b64 v[184:185], 11, v[184:185]
	v_lshl_add_u64 v[184:185], v[158:159], 0, v[184:185]
	global_load_dwordx4 v[220:223], v[184:185], off
	global_load_dwordx4 v[224:227], v[184:185], off offset:256
	ds_read_b32 v0, v161 offset:16512
	v_or_b32_e32 v136, 32, v162
	v_add_u32_e32 v130, s10, v136
	v_ashrrev_i32_e32 v131, 31, v130
	v_lshlrev_b64 v[130:131], 11, v[130:131]
	s_waitcnt lgkmcnt(0)
	v_pk_mul_f32 v[112:113], v[112:113], v[0:1] op_sel_hi:[1,0]
	v_pk_mul_f32 v[110:111], v[110:111], v[0:1] op_sel_hi:[1,0]
	v_pk_mul_f32 v[106:107], v[106:107], v[0:1] op_sel_hi:[1,0]
	v_pk_mul_f32 v[108:109], v[108:109], v[0:1] op_sel_hi:[1,0]
	v_pk_mul_f32 v[102:103], v[102:103], v[0:1] op_sel_hi:[1,0]
	v_pk_mul_f32 v[104:105], v[104:105], v[0:1] op_sel_hi:[1,0]
	v_pk_mul_f32 v[98:99], v[98:99], v[0:1] op_sel_hi:[1,0]
	v_pk_mul_f32 v[100:101], v[100:101], v[0:1] op_sel_hi:[1,0]
	v_lshlrev_b32_e32 v132, 16, v122
	v_and_b32_e32 v133, 0xffff0000, v122
	v_lshlrev_b32_e32 v122, 16, v123
	v_and_b32_e32 v123, 0xffff0000, v123
	v_lshlrev_b32_e32 v134, 16, v124
	v_and_b32_e32 v135, 0xffff0000, v124
	v_lshlrev_b32_e32 v124, 16, v125
	v_and_b32_e32 v125, 0xffff0000, v125
	v_pk_fma_f32 v[112:113], v[96:97], v[112:113], v[122:123]
	v_pk_fma_f32 v[110:111], v[94:95], v[110:111], v[132:133]
	v_pk_fma_f32 v[122:123], v[92:93], v[108:109], v[124:125]
	v_pk_fma_f32 v[124:125], v[90:91], v[106:107], v[134:135]
	v_mul_f32_e32 v109, v113, v113
	v_cvt_pk_bf16_f32 v106, v110, v111
	v_cvt_pk_bf16_f32 v107, v112, v113
	v_mul_f32_e32 v108, v111, v111
	v_fmac_f32_e32 v109, v112, v112
	v_mul_f32_e32 v111, v125, v125
	v_mul_f32_e32 v112, v123, v123
	v_fmac_f32_e32 v108, v110, v110
	v_fmac_f32_e32 v111, v124, v124
	v_fmac_f32_e32 v112, v122, v122
	v_add_f32_e32 v110, v108, v109
	v_add_f32_e32 v111, v111, v112
	v_cvt_pk_bf16_f32 v108, v124, v125
	v_add_f32_e32 v124, v111, v110
	v_lshl_add_u64 v[110:111], s[2:3], 0, v[130:131]
	v_cvt_pk_bf16_f32 v109, v122, v123
	v_lshl_add_u64 v[110:111], v[110:111], 0, v[156:157]
	global_store_dwordx4 v[110:111], v[106:109], off
	v_lshlrev_b32_e32 v112, 16, v128
	v_and_b32_e32 v113, 0xffff0000, v128
	v_lshlrev_b32_e32 v106, 16, v126
	v_and_b32_e32 v107, 0xffff0000, v126
	v_lshlrev_b32_e32 v108, 16, v127
	v_and_b32_e32 v109, 0xffff0000, v127
	v_lshlrev_b32_e32 v122, 16, v129
	v_and_b32_e32 v123, 0xffff0000, v129
	v_pk_fma_f32 v[104:105], v[88:89], v[104:105], v[108:109]
	v_pk_fma_f32 v[102:103], v[86:87], v[102:103], v[106:107]
	v_pk_fma_f32 v[106:107], v[84:85], v[100:101], v[122:123]
	v_pk_fma_f32 v[108:109], v[82:83], v[98:99], v[112:113]
	v_mul_f32_e32 v0, v103, v103
	v_mul_f32_e32 v100, v105, v105
	v_cvt_pk_bf16_f32 v98, v102, v103
	v_fmac_f32_e32 v0, v102, v102
	v_fmac_f32_e32 v100, v104, v104
	v_mul_f32_e32 v102, v109, v109
	v_mul_f32_e32 v103, v107, v107
	v_add_f32_e32 v0, v0, v100
	v_fmac_f32_e32 v102, v108, v108
	v_fmac_f32_e32 v103, v106, v106
	v_cvt_pk_bf16_f32 v99, v104, v105
	v_add_f32_e32 v0, v0, v124
	v_cvt_pk_bf16_f32 v100, v108, v109
	v_cvt_pk_bf16_f32 v101, v106, v107
	v_add_f32_e32 v102, v102, v103
	v_add_f32_e32 v0, v102, v0
	global_store_dwordx4 v[110:111], v[98:101], off offset:256
	v_lshlrev_b32_e32 v102, 16, v119
	v_and_b32_e32 v103, 0xffff0000, v119
	v_lshl_add_u32 v98, v136, 6, v163
	ds_write_b32 v98, v0
	ds_read_b32 v0, v161 offset:16576
	v_lshlrev_b32_e32 v100, 16, v118
	v_and_b32_e32 v101, 0xffff0000, v118
	v_lshlrev_b32_e32 v104, 16, v120
	v_and_b32_e32 v105, 0xffff0000, v120
	s_waitcnt lgkmcnt(0)
	v_pk_mul_f32 v[80:81], v[80:81], v[0:1] op_sel_hi:[1,0]
	v_lshlrev_b32_e32 v106, 16, v121
	v_and_b32_e32 v107, 0xffff0000, v121
	v_pk_mul_f32 v[78:79], v[78:79], v[0:1] op_sel_hi:[1,0]
	v_pk_fma_f32 v[80:81], v[96:97], v[80:81], v[102:103]
	v_pk_mul_f32 v[74:75], v[74:75], v[0:1] op_sel_hi:[1,0]
	v_pk_mul_f32 v[76:77], v[76:77], v[0:1] op_sel_hi:[1,0]
	v_or_b32_e32 v108, 48, v162
	v_pk_fma_f32 v[78:79], v[94:95], v[78:79], v[100:101]
	v_pk_fma_f32 v[100:101], v[92:93], v[76:77], v[106:107]
	v_pk_fma_f32 v[102:103], v[90:91], v[74:75], v[104:105]
	v_mul_f32_e32 v77, v81, v81
	v_add_u32_e32 v98, s10, v108
	v_cvt_pk_bf16_f32 v74, v78, v79
	v_cvt_pk_bf16_f32 v75, v80, v81
	v_mul_f32_e32 v76, v79, v79
	v_fmac_f32_e32 v77, v80, v80
	v_mul_f32_e32 v79, v103, v103
	v_mul_f32_e32 v80, v101, v101
	v_ashrrev_i32_e32 v99, 31, v98
	v_fmac_f32_e32 v76, v78, v78
	v_fmac_f32_e32 v79, v102, v102
	v_fmac_f32_e32 v80, v100, v100
	v_lshlrev_b64 v[98:99], 11, v[98:99]
	v_add_f32_e32 v78, v76, v77
	v_add_f32_e32 v79, v79, v80
	v_cvt_pk_bf16_f32 v77, v100, v101
	v_add_f32_e32 v100, v79, v78
	v_lshl_add_u64 v[78:79], s[2:3], 0, v[98:99]
	v_cvt_pk_bf16_f32 v76, v102, v103
	v_lshl_add_u64 v[78:79], v[78:79], 0, v[156:157]
	global_store_dwordx4 v[78:79], v[74:77], off
	v_pk_mul_f32 v[70:71], v[70:71], v[0:1] op_sel_hi:[1,0]
	v_pk_mul_f32 v[72:73], v[72:73], v[0:1] op_sel_hi:[1,0]
	v_lshlrev_b32_e32 v74, 16, v114
	v_and_b32_e32 v75, 0xffff0000, v114
	v_lshlrev_b32_e32 v76, 16, v115
	v_and_b32_e32 v77, 0xffff0000, v115
	v_lshlrev_b32_e32 v80, 16, v116
	v_and_b32_e32 v81, 0xffff0000, v116
	v_lshlrev_b32_e32 v98, 16, v117
	v_and_b32_e32 v99, 0xffff0000, v117
	v_pk_fma_f32 v[72:73], v[88:89], v[72:73], v[76:77]
	v_pk_fma_f32 v[70:71], v[86:87], v[70:71], v[74:75]
	v_pk_mul_f32 v[66:67], v[66:67], v[0:1] op_sel_hi:[1,0]
	v_pk_mul_f32 v[68:69], v[68:69], v[0:1] op_sel_hi:[1,0]
	v_pk_fma_f32 v[76:77], v[82:83], v[66:67], v[80:81]
	v_pk_fma_f32 v[74:75], v[84:85], v[68:69], v[98:99]
	v_mul_f32_e32 v0, v71, v71
	v_mul_f32_e32 v68, v73, v73
	v_cvt_pk_bf16_f32 v66, v70, v71
	v_fmac_f32_e32 v0, v70, v70
	v_fmac_f32_e32 v68, v72, v72
	v_mul_f32_e32 v70, v77, v77
	v_mul_f32_e32 v71, v75, v75
	v_add_f32_e32 v0, v0, v68
	v_fmac_f32_e32 v70, v76, v76
	v_fmac_f32_e32 v71, v74, v74
	v_cvt_pk_bf16_f32 v67, v72, v73
	v_add_f32_e32 v0, v0, v100
	v_cvt_pk_bf16_f32 v68, v76, v77
	v_cvt_pk_bf16_f32 v69, v74, v75
	v_add_f32_e32 v70, v70, v71
	v_add_f32_e32 v0, v70, v0
	global_store_dwordx4 v[78:79], v[66:69], off offset:256
	s_nop 1
	v_lshl_add_u32 v66, v108, 6, v163
	ds_write_b32 v66, v0
	s_waitcnt vmcnt(4)
	v_mov_b32_e32 v74, v212
	v_mov_b32_e32 v75, v213
	v_mov_b32_e32 v76, v214
	v_mov_b32_e32 v77, v215
	v_mov_b32_e32 v78, v216
	v_mov_b32_e32 v79, v217
	v_mov_b32_e32 v80, v218
	v_mov_b32_e32 v81, v219
	v_mov_b32_e32 v70, v220
	v_mov_b32_e32 v71, v221
	v_mov_b32_e32 v72, v222
	v_mov_b32_e32 v73, v223
	v_mov_b32_e32 v66, v224
	v_mov_b32_e32 v67, v225
	v_mov_b32_e32 v68, v226
	v_mov_b32_e32 v69, v227
	v_add_u32_e32 v184, 0xa0, v160
	v_ashrrev_i32_e32 v185, 31, v184
	v_lshlrev_b64 v[184:185], 11, v[184:185]
	v_lshl_add_u64 v[184:185], v[158:159], 0, v[184:185]
	global_load_dwordx4 v[212:215], v[184:185], off
	global_load_dwordx4 v[216:219], v[184:185], off offset:256
	v_add_u32_e32 v184, 0xb0, v160
	v_ashrrev_i32_e32 v185, 31, v184
	v_lshlrev_b64 v[184:185], 11, v[184:185]
	v_lshl_add_u64 v[184:185], v[158:159], 0, v[184:185]
	global_load_dwordx4 v[220:223], v[184:185], off
	global_load_dwordx4 v[224:227], v[184:185], off offset:256
	ds_read_b32 v0, v161 offset:16896
	v_add_u32_e32 v104, 0x80, v162
	v_add_u32_e32 v98, s10, v104
	v_ashrrev_i32_e32 v99, 31, v98
	v_lshlrev_b64 v[98:99], 11, v[98:99]
	s_waitcnt lgkmcnt(0)
	v_pk_mul_f32 v[64:65], v[64:65], v[0:1] op_sel_hi:[1,0]
	v_pk_mul_f32 v[62:63], v[62:63], v[0:1] op_sel_hi:[1,0]
	v_pk_mul_f32 v[58:59], v[58:59], v[0:1] op_sel_hi:[1,0]
	v_pk_mul_f32 v[60:61], v[60:61], v[0:1] op_sel_hi:[1,0]
	v_pk_mul_f32 v[54:55], v[54:55], v[0:1] op_sel_hi:[1,0]
	v_pk_mul_f32 v[56:57], v[56:57], v[0:1] op_sel_hi:[1,0]
	v_pk_mul_f32 v[50:51], v[50:51], v[0:1] op_sel_hi:[1,0]
	v_pk_mul_f32 v[52:53], v[52:53], v[0:1] op_sel_hi:[1,0]
	v_lshlrev_b32_e32 v100, 16, v74
	v_and_b32_e32 v101, 0xffff0000, v74
	v_lshlrev_b32_e32 v74, 16, v75
	v_and_b32_e32 v75, 0xffff0000, v75
	v_lshlrev_b32_e32 v102, 16, v76
	v_and_b32_e32 v103, 0xffff0000, v76
	v_lshlrev_b32_e32 v76, 16, v77
	v_and_b32_e32 v77, 0xffff0000, v77
	v_pk_fma_f32 v[64:65], v[96:97], v[64:65], v[74:75]
	v_pk_fma_f32 v[62:63], v[94:95], v[62:63], v[100:101]
	v_pk_fma_f32 v[74:75], v[92:93], v[60:61], v[76:77]
	v_pk_fma_f32 v[76:77], v[90:91], v[58:59], v[102:103]
	v_mul_f32_e32 v61, v65, v65
	v_cvt_pk_bf16_f32 v58, v62, v63
	v_cvt_pk_bf16_f32 v59, v64, v65
	v_mul_f32_e32 v60, v63, v63
	v_fmac_f32_e32 v61, v64, v64
	v_mul_f32_e32 v63, v77, v77
	v_mul_f32_e32 v64, v75, v75
	v_fmac_f32_e32 v60, v62, v62
	v_fmac_f32_e32 v63, v76, v76
	v_fmac_f32_e32 v64, v74, v74
	v_add_f32_e32 v62, v60, v61
	v_add_f32_e32 v63, v63, v64
	v_cvt_pk_bf16_f32 v60, v76, v77
	v_add_f32_e32 v76, v63, v62
	v_lshl_add_u64 v[62:63], s[2:3], 0, v[98:99]
	v_cvt_pk_bf16_f32 v61, v74, v75
	v_lshl_add_u64 v[62:63], v[62:63], 0, v[156:157]
	global_store_dwordx4 v[62:63], v[58:61], off
	v_lshlrev_b32_e32 v64, 16, v80
	v_and_b32_e32 v65, 0xffff0000, v80
	v_lshlrev_b32_e32 v58, 16, v78
	v_and_b32_e32 v59, 0xffff0000, v78
	v_lshlrev_b32_e32 v60, 16, v79
	v_and_b32_e32 v61, 0xffff0000, v79
	v_lshlrev_b32_e32 v74, 16, v81
	v_and_b32_e32 v75, 0xffff0000, v81
	v_pk_fma_f32 v[56:57], v[88:89], v[56:57], v[60:61]
	v_pk_fma_f32 v[54:55], v[86:87], v[54:55], v[58:59]
	v_pk_fma_f32 v[58:59], v[84:85], v[52:53], v[74:75]
	v_pk_fma_f32 v[60:61], v[82:83], v[50:51], v[64:65]
	v_mul_f32_e32 v0, v55, v55
	v_mul_f32_e32 v52, v57, v57
	v_cvt_pk_bf16_f32 v50, v54, v55
	v_fmac_f32_e32 v0, v54, v54
	v_fmac_f32_e32 v52, v56, v56
	v_mul_f32_e32 v54, v61, v61
	v_mul_f32_e32 v55, v59, v59
	v_add_f32_e32 v0, v0, v52
	v_fmac_f32_e32 v54, v60, v60
	v_fmac_f32_e32 v55, v58, v58
	v_cvt_pk_bf16_f32 v51, v56, v57
	v_add_f32_e32 v0, v0, v76
	v_cvt_pk_bf16_f32 v52, v60, v61
	v_cvt_pk_bf16_f32 v53, v58, v59
	v_add_f32_e32 v54, v54, v55
	v_add_f32_e32 v0, v54, v0
	global_store_dwordx4 v[62:63], v[50:53], off offset:256
	v_lshlrev_b32_e32 v54, 16, v71
	v_and_b32_e32 v55, 0xffff0000, v71
	v_lshl_add_u32 v50, v104, 6, v163
	ds_write_b32 v50, v0
	ds_read_b32 v0, v161 offset:16960
	v_lshlrev_b32_e32 v52, 16, v70
	v_and_b32_e32 v53, 0xffff0000, v70
	v_lshlrev_b32_e32 v56, 16, v72
	v_and_b32_e32 v57, 0xffff0000, v72
	s_waitcnt lgkmcnt(0)
	v_pk_mul_f32 v[48:49], v[48:49], v[0:1] op_sel_hi:[1,0]
	v_lshlrev_b32_e32 v58, 16, v73
	v_and_b32_e32 v59, 0xffff0000, v73
	v_pk_mul_f32 v[46:47], v[46:47], v[0:1] op_sel_hi:[1,0]
	v_pk_fma_f32 v[48:49], v[96:97], v[48:49], v[54:55]
	v_pk_mul_f32 v[42:43], v[42:43], v[0:1] op_sel_hi:[1,0]
	v_pk_mul_f32 v[44:45], v[44:45], v[0:1] op_sel_hi:[1,0]
	v_add_u32_e32 v60, 0x90, v162
	v_pk_fma_f32 v[46:47], v[94:95], v[46:47], v[52:53]
	v_pk_fma_f32 v[52:53], v[92:93], v[44:45], v[58:59]
	v_pk_fma_f32 v[54:55], v[90:91], v[42:43], v[56:57]
	v_mul_f32_e32 v45, v49, v49
	v_add_u32_e32 v50, s10, v60
	v_cvt_pk_bf16_f32 v42, v46, v47
	v_cvt_pk_bf16_f32 v43, v48, v49
	v_mul_f32_e32 v44, v47, v47
	v_fmac_f32_e32 v45, v48, v48
	v_mul_f32_e32 v47, v55, v55
	v_mul_f32_e32 v48, v53, v53
	v_ashrrev_i32_e32 v51, 31, v50
	v_fmac_f32_e32 v44, v46, v46
	v_fmac_f32_e32 v47, v54, v54
	v_fmac_f32_e32 v48, v52, v52
	v_lshlrev_b64 v[50:51], 11, v[50:51]
	v_add_f32_e32 v46, v44, v45
	v_add_f32_e32 v47, v47, v48
	v_cvt_pk_bf16_f32 v45, v52, v53
	v_add_f32_e32 v52, v47, v46
	v_lshl_add_u64 v[46:47], s[2:3], 0, v[50:51]
	v_cvt_pk_bf16_f32 v44, v54, v55
	v_lshl_add_u64 v[46:47], v[46:47], 0, v[156:157]
	global_store_dwordx4 v[46:47], v[42:45], off
	v_pk_mul_f32 v[38:39], v[38:39], v[0:1] op_sel_hi:[1,0]
	v_pk_mul_f32 v[40:41], v[40:41], v[0:1] op_sel_hi:[1,0]
	v_lshlrev_b32_e32 v42, 16, v66
	v_and_b32_e32 v43, 0xffff0000, v66
	v_lshlrev_b32_e32 v44, 16, v67
	v_and_b32_e32 v45, 0xffff0000, v67
	v_lshlrev_b32_e32 v48, 16, v68
	v_and_b32_e32 v49, 0xffff0000, v68
	v_lshlrev_b32_e32 v50, 16, v69
	v_and_b32_e32 v51, 0xffff0000, v69
	v_pk_fma_f32 v[40:41], v[88:89], v[40:41], v[44:45]
	v_pk_fma_f32 v[38:39], v[86:87], v[38:39], v[42:43]
	v_pk_mul_f32 v[34:35], v[34:35], v[0:1] op_sel_hi:[1,0]
	v_pk_mul_f32 v[36:37], v[36:37], v[0:1] op_sel_hi:[1,0]
	v_pk_fma_f32 v[44:45], v[82:83], v[34:35], v[48:49]
	v_pk_fma_f32 v[42:43], v[84:85], v[36:37], v[50:51]
	v_mul_f32_e32 v0, v39, v39
	v_mul_f32_e32 v36, v41, v41
	v_cvt_pk_bf16_f32 v34, v38, v39
	v_fmac_f32_e32 v0, v38, v38
	v_fmac_f32_e32 v36, v40, v40
	v_mul_f32_e32 v38, v45, v45
	v_mul_f32_e32 v39, v43, v43
	v_add_f32_e32 v0, v0, v36
	v_fmac_f32_e32 v38, v44, v44
	v_fmac_f32_e32 v39, v42, v42
	v_cvt_pk_bf16_f32 v35, v40, v41
	v_add_f32_e32 v0, v0, v52
	v_cvt_pk_bf16_f32 v36, v44, v45
	v_cvt_pk_bf16_f32 v37, v42, v43
	v_add_f32_e32 v38, v38, v39
	v_add_f32_e32 v0, v38, v0
	global_store_dwordx4 v[46:47], v[34:37], off offset:256
	s_nop 1
	v_lshl_add_u32 v34, v60, 6, v163
	ds_write_b32 v34, v0
	s_waitcnt vmcnt(4)
	v_mov_b32_e32 v42, v212
	v_mov_b32_e32 v43, v213
	v_mov_b32_e32 v44, v214
	v_mov_b32_e32 v45, v215
	v_mov_b32_e32 v46, v216
	v_mov_b32_e32 v47, v217
	v_mov_b32_e32 v48, v218
	v_mov_b32_e32 v49, v219
	v_mov_b32_e32 v38, v220
	v_mov_b32_e32 v39, v221
	v_mov_b32_e32 v40, v222
	v_mov_b32_e32 v41, v223
	v_mov_b32_e32 v34, v224
	v_mov_b32_e32 v35, v225
	v_mov_b32_e32 v36, v226
	v_mov_b32_e32 v37, v227
	ds_read_b32 v0, v161 offset:17024
	v_add_u32_e32 v56, 0xa0, v162
	v_add_u32_e32 v50, s10, v56
	v_ashrrev_i32_e32 v51, 31, v50
	v_lshlrev_b64 v[50:51], 11, v[50:51]
	s_waitcnt lgkmcnt(0)
	v_pk_mul_f32 v[32:33], v[32:33], v[0:1] op_sel_hi:[1,0]
	v_pk_mul_f32 v[30:31], v[30:31], v[0:1] op_sel_hi:[1,0]
	v_pk_mul_f32 v[26:27], v[26:27], v[0:1] op_sel_hi:[1,0]
	v_pk_mul_f32 v[28:29], v[28:29], v[0:1] op_sel_hi:[1,0]
	v_pk_mul_f32 v[22:23], v[22:23], v[0:1] op_sel_hi:[1,0]
	v_pk_mul_f32 v[24:25], v[24:25], v[0:1] op_sel_hi:[1,0]
	v_pk_mul_f32 v[18:19], v[18:19], v[0:1] op_sel_hi:[1,0]
	v_pk_mul_f32 v[20:21], v[20:21], v[0:1] op_sel_hi:[1,0]
	v_lshlrev_b32_e32 v52, 16, v42
	v_and_b32_e32 v53, 0xffff0000, v42
	v_lshlrev_b32_e32 v42, 16, v43
	v_and_b32_e32 v43, 0xffff0000, v43
	v_lshlrev_b32_e32 v54, 16, v44
	v_and_b32_e32 v55, 0xffff0000, v44
	v_lshlrev_b32_e32 v44, 16, v45
	v_and_b32_e32 v45, 0xffff0000, v45
	v_pk_fma_f32 v[32:33], v[96:97], v[32:33], v[42:43]
	v_pk_fma_f32 v[30:31], v[94:95], v[30:31], v[52:53]
	v_pk_fma_f32 v[42:43], v[92:93], v[28:29], v[44:45]
	v_pk_fma_f32 v[44:45], v[90:91], v[26:27], v[54:55]
	v_mul_f32_e32 v29, v33, v33
	v_cvt_pk_bf16_f32 v26, v30, v31
	v_cvt_pk_bf16_f32 v27, v32, v33
	v_mul_f32_e32 v28, v31, v31
	v_fmac_f32_e32 v29, v32, v32
	v_mul_f32_e32 v31, v45, v45
	v_mul_f32_e32 v32, v43, v43
	v_fmac_f32_e32 v28, v30, v30
	v_fmac_f32_e32 v31, v44, v44
	v_fmac_f32_e32 v32, v42, v42
	v_add_f32_e32 v30, v28, v29
	v_add_f32_e32 v31, v31, v32
	v_cvt_pk_bf16_f32 v28, v44, v45
	v_add_f32_e32 v44, v31, v30
	v_lshl_add_u64 v[30:31], s[2:3], 0, v[50:51]
	v_cvt_pk_bf16_f32 v29, v42, v43
	v_lshl_add_u64 v[30:31], v[30:31], 0, v[156:157]
	global_store_dwordx4 v[30:31], v[26:29], off
	v_lshlrev_b32_e32 v32, 16, v48
	v_and_b32_e32 v33, 0xffff0000, v48
	v_lshlrev_b32_e32 v26, 16, v46
	v_and_b32_e32 v27, 0xffff0000, v46
	v_lshlrev_b32_e32 v28, 16, v47
	v_and_b32_e32 v29, 0xffff0000, v47
	v_lshlrev_b32_e32 v42, 16, v49
	v_and_b32_e32 v43, 0xffff0000, v49
	v_pk_fma_f32 v[24:25], v[88:89], v[24:25], v[28:29]
	v_pk_fma_f32 v[22:23], v[86:87], v[22:23], v[26:27]
	v_pk_fma_f32 v[26:27], v[84:85], v[20:21], v[42:43]
	v_pk_fma_f32 v[28:29], v[82:83], v[18:19], v[32:33]
	v_mul_f32_e32 v0, v23, v23
	v_mul_f32_e32 v20, v25, v25
	v_cvt_pk_bf16_f32 v18, v22, v23
	v_fmac_f32_e32 v0, v22, v22
	v_fmac_f32_e32 v20, v24, v24
	v_mul_f32_e32 v22, v29, v29
	v_mul_f32_e32 v23, v27, v27
	v_add_f32_e32 v0, v0, v20
	v_fmac_f32_e32 v22, v28, v28
	v_fmac_f32_e32 v23, v26, v26
	v_cvt_pk_bf16_f32 v19, v24, v25
	v_add_f32_e32 v0, v0, v44
	v_cvt_pk_bf16_f32 v20, v28, v29
	v_cvt_pk_bf16_f32 v21, v26, v27
	v_add_f32_e32 v22, v22, v23
	v_add_f32_e32 v0, v22, v0
	global_store_dwordx4 v[30:31], v[18:21], off offset:256
	v_lshlrev_b32_e32 v22, 16, v39
	v_and_b32_e32 v23, 0xffff0000, v39
	v_lshl_add_u32 v18, v56, 6, v163
	ds_write_b32 v18, v0
	ds_read_b32 v0, v161 offset:17088
	v_lshlrev_b32_e32 v20, 16, v38
	v_and_b32_e32 v21, 0xffff0000, v38
	v_lshlrev_b32_e32 v24, 16, v40
	v_and_b32_e32 v25, 0xffff0000, v40
	s_waitcnt lgkmcnt(0)
	v_pk_mul_f32 v[16:17], v[16:17], v[0:1] op_sel_hi:[1,0]
	v_lshlrev_b32_e32 v26, 16, v41
	v_and_b32_e32 v27, 0xffff0000, v41
	v_pk_mul_f32 v[14:15], v[14:15], v[0:1] op_sel_hi:[1,0]
	v_pk_fma_f32 v[16:17], v[96:97], v[16:17], v[22:23]
	v_pk_mul_f32 v[10:11], v[10:11], v[0:1] op_sel_hi:[1,0]
	v_pk_mul_f32 v[12:13], v[12:13], v[0:1] op_sel_hi:[1,0]
	v_add_u32_e32 v28, 0xb0, v162
	v_pk_fma_f32 v[14:15], v[94:95], v[14:15], v[20:21]
	v_pk_fma_f32 v[20:21], v[92:93], v[12:13], v[26:27]
	v_pk_fma_f32 v[22:23], v[90:91], v[10:11], v[24:25]
	v_mul_f32_e32 v13, v17, v17
	v_add_u32_e32 v18, s10, v28
	v_cvt_pk_bf16_f32 v10, v14, v15
	v_cvt_pk_bf16_f32 v11, v16, v17
	v_mul_f32_e32 v12, v15, v15
	v_fmac_f32_e32 v13, v16, v16
	v_mul_f32_e32 v15, v23, v23
	v_mul_f32_e32 v16, v21, v21
	v_ashrrev_i32_e32 v19, 31, v18
	v_fmac_f32_e32 v12, v14, v14
	v_fmac_f32_e32 v15, v22, v22
	v_fmac_f32_e32 v16, v20, v20
	v_lshlrev_b64 v[18:19], 11, v[18:19]
	v_add_f32_e32 v14, v12, v13
	v_add_f32_e32 v15, v15, v16
	v_cvt_pk_bf16_f32 v13, v20, v21
	v_add_f32_e32 v20, v15, v14
	v_lshl_add_u64 v[14:15], s[2:3], 0, v[18:19]
	v_cvt_pk_bf16_f32 v12, v22, v23
	v_lshl_add_u64 v[14:15], v[14:15], 0, v[156:157]
	global_store_dwordx4 v[14:15], v[10:13], off
	v_pk_mul_f32 v[6:7], v[6:7], v[0:1] op_sel_hi:[1,0]
	v_pk_mul_f32 v[8:9], v[8:9], v[0:1] op_sel_hi:[1,0]
	v_lshlrev_b32_e32 v10, 16, v34
	v_and_b32_e32 v11, 0xffff0000, v34
	v_lshlrev_b32_e32 v12, 16, v35
	v_and_b32_e32 v13, 0xffff0000, v35
	v_lshlrev_b32_e32 v16, 16, v36
	v_and_b32_e32 v17, 0xffff0000, v36
	v_lshlrev_b32_e32 v18, 16, v37
	v_and_b32_e32 v19, 0xffff0000, v37
	v_pk_fma_f32 v[8:9], v[88:89], v[8:9], v[12:13]
	v_pk_fma_f32 v[6:7], v[86:87], v[6:7], v[10:11]
	v_pk_mul_f32 v[2:3], v[2:3], v[0:1] op_sel_hi:[1,0]
	v_pk_mul_f32 v[4:5], v[4:5], v[0:1] op_sel_hi:[1,0]
	v_pk_fma_f32 v[12:13], v[82:83], v[2:3], v[16:17]
	v_pk_fma_f32 v[10:11], v[84:85], v[4:5], v[18:19]
	v_mul_f32_e32 v0, v7, v7
	v_mul_f32_e32 v4, v9, v9
	v_cvt_pk_bf16_f32 v2, v6, v7
	v_fmac_f32_e32 v0, v6, v6
	v_fmac_f32_e32 v4, v8, v8
	v_mul_f32_e32 v6, v13, v13
	v_mul_f32_e32 v7, v11, v11
	v_add_f32_e32 v0, v0, v4
	v_fmac_f32_e32 v6, v12, v12
	v_fmac_f32_e32 v7, v10, v10
	v_cvt_pk_bf16_f32 v3, v8, v9
	v_add_f32_e32 v0, v0, v20
	v_cvt_pk_bf16_f32 v4, v12, v13
	v_cvt_pk_bf16_f32 v5, v10, v11
	v_add_f32_e32 v6, v6, v7
	v_add_f32_e32 v0, v6, v0
	global_store_dwordx4 v[14:15], v[2:5], off offset:256
	s_nop 1
	v_lshl_add_u32 v2, v28, 6, v163
	ds_write_b32 v2, v0
	s_waitcnt lgkmcnt(0)
	s_barrier
	s_and_saveexec_b64 s[2:3], s[0:1]
	s_cbranch_execz .LBB0_1545
	ds_read_b128 v[2:5], v164
	ds_read_b128 v[6:9], v164 offset:32
	ds_read_b128 v[10:13], v164 offset:16
	ds_read_b128 v[14:17], v164 offset:48
	v_readlane_b32 s0, v252, 16
	s_waitcnt lgkmcnt(3)
	v_mov_b32_e32 v18, v2
	s_waitcnt lgkmcnt(2)
	v_mov_b32_e32 v19, v6
	v_mov_b32_e32 v6, v3
	v_pk_add_f32 v[2:3], v[18:19], v[6:7]
	v_mov_b32_e32 v6, v4
	v_mov_b32_e32 v7, v8
	v_mov_b32_e32 v8, v5
	v_pk_add_f32 v[4:5], v[6:7], v[8:9]
	s_waitcnt lgkmcnt(1)
	v_mov_b32_e32 v6, v12
	v_pk_add_f32 v[2:3], v[2:3], v[4:5]
	v_mov_b32_e32 v4, v10
	s_waitcnt lgkmcnt(0)
	v_mov_b32_e32 v5, v14
	v_mov_b32_e32 v14, v11
	v_mov_b32_e32 v7, v16
	v_mov_b32_e32 v16, v13
	v_pk_add_f32 v[4:5], v[4:5], v[14:15]
	v_pk_add_f32 v[6:7], v[6:7], v[16:17]
	v_readlane_b32 s1, v252, 17
	v_pk_add_f32 v[4:5], v[4:5], v[6:7]
	s_ashr_i32 s5, s4, 31
	v_pk_add_f32 v[2:3], v[2:3], v[4:5]
	v_lshl_add_u64 v[4:5], v[154:155], 4, s[0:1]
	v_pk_add_f32 v[2:3], v[2:3], v[2:3] op_sel:[0,1] op_sel_hi:[1,0]
	v_lshl_add_u64 v[4:5], s[4:5], 2, v[4:5]
	global_store_dword v[4:5], v2, off sc1
